# speedup vs baseline: 1.0517x; 1.0517x over previous
.Lno_anc:
	s_or_b64 exec, exec, s[8:9]
	v_mov_b32_e32 v7, 0x80
	s_and_b32 s27, s2, 0xf8
	s_cmp_lg_u32 s27, 0
	s_cbranch_scc1 .Lno_touch
	v_lshlrev_b32_e32 v9, 4, v6
	s_mov_b64 exec, 1
	global_load_dword v24, v9, s[16:17] nt
	global_load_dword v25, v9, s[18:19] nt
	s_mov_b64 exec, -1
	s_waitcnt vmcnt(2)
	s_branch .Lmask_ready
.Lno_touch:
	s_waitcnt vmcnt(0)
.Lmask_ready:
	s_sub_u32 s26, 0x1ff, s2
	s_mul_i32 s26, s26, 7
	s_lshr_b32 s26, s26, 6
	s_min_u32 s26, s26, 64
	s_cmp_eq_u32 s26, 0
	s_cbranch_scc1 .Lhold_done

	.amdhsa_kernel _Z12giou_partialPK15HIP_vector_typeIfLj4EES2_S2_PKiPS_IfLj2EE
		.amdhsa_group_segment_fixed_size 24704
		.amdhsa_private_segment_fixed_size 0
		.amdhsa_kernarg_size 40
		.amdhsa_user_sgpr_count 2
		.amdhsa_user_sgpr_dispatch_ptr 0
		.amdhsa_user_sgpr_queue_ptr 0
		.amdhsa_user_sgpr_kernarg_segment_ptr 1
		.amdhsa_user_sgpr_dispatch_id 0
		.amdhsa_user_sgpr_kernarg_preload_length 0
		.amdhsa_user_sgpr_kernarg_preload_offset 0
		.amdhsa_user_sgpr_private_segment_size 0
		.amdhsa_uses_dynamic_stack 0
		.amdhsa_enable_private_segment 0
		.amdhsa_system_sgpr_workgroup_id_x 1
		.amdhsa_system_sgpr_workgroup_id_y 0
		.amdhsa_system_sgpr_workgroup_id_z 0
		.amdhsa_system_sgpr_workgroup_info 0
		.amdhsa_system_vgpr_workitem_id 0
		.amdhsa_next_free_vgpr 26
		.amdhsa_next_free_sgpr 28
		.amdhsa_accum_offset 28
		.amdhsa_reserve_vcc 1
		.amdhsa_float_round_mode_32 0
		.amdhsa_float_round_mode_16_64 0
		.amdhsa_float_denorm_mode_32 3
		.amdhsa_float_denorm_mode_16_64 3
		.amdhsa_dx10_clamp 1
		.amdhsa_ieee_mode 1
		.amdhsa_fp16_overflow 0
		.amdhsa_tg_split 0
		.amdhsa_exception_fp_ieee_invalid_op 0
		.amdhsa_exception_fp_denorm_src 0
		.amdhsa_exception_fp_ieee_div_zero 0
		.amdhsa_exception_fp_ieee_overflow 0
		.amdhsa_exception_fp_ieee_underflow 0
		.amdhsa_exception_fp_ieee_inexact 0
		.amdhsa_exception_int_div_zero 0
	.end_amdhsa_kernel

.Lfunc_end0:
	.size	_Z12giou_partialPK15HIP_vector_typeIfLj4EES2_S2_PKiPS_IfLj2EE, .Lfunc_end0-_Z12giou_partialPK15HIP_vector_typeIfLj4EES2_S2_PKiPS_IfLj2EE
	.set _Z12giou_partialPK15HIP_vector_typeIfLj4EES2_S2_PKiPS_IfLj2EE.num_vgpr, 26
	.set _Z12giou_partialPK15HIP_vector_typeIfLj4EES2_S2_PKiPS_IfLj2EE.num_agpr, 0
	.set _Z12giou_partialPK15HIP_vector_typeIfLj4EES2_S2_PKiPS_IfLj2EE.numbered_sgpr, 28
	.set _Z12giou_partialPK15HIP_vector_typeIfLj4EES2_S2_PKiPS_IfLj2EE.num_named_barrier, 0
	.set _Z12giou_partialPK15HIP_vector_typeIfLj4EES2_S2_PKiPS_IfLj2EE.private_seg_size, 0
	.set _Z12giou_partialPK15HIP_vector_typeIfLj4EES2_S2_PKiPS_IfLj2EE.uses_vcc, 1
	.set _Z12giou_partialPK15HIP_vector_typeIfLj4EES2_S2_PKiPS_IfLj2EE.uses_flat_scratch, 0
	.set _Z12giou_partialPK15HIP_vector_typeIfLj4EES2_S2_PKiPS_IfLj2EE.has_dyn_sized_stack, 0
	.set _Z12giou_partialPK15HIP_vector_typeIfLj4EES2_S2_PKiPS_IfLj2EE.has_recursion, 0
	.set _Z12giou_partialPK15HIP_vector_typeIfLj4EES2_S2_PKiPS_IfLj2EE.has_indirect_call, 0

amdhsa.kernels:
  - .agpr_count:     0
    .args:
      - .actual_access:  read_only
        .address_space:  global
        .offset:         0
        .size:           8
        .value_kind:     global_buffer
      - .actual_access:  read_only
        .address_space:  global
        .offset:         8
        .size:           8
        .value_kind:     global_buffer
      - .actual_access:  read_only
        .address_space:  global
        .offset:         16
        .size:           8
        .value_kind:     global_buffer
      - .actual_access:  read_only
        .address_space:  global
        .offset:         24
        .size:           8
        .value_kind:     global_buffer
      - .actual_access:  write_only
        .address_space:  global
        .offset:         32
        .size:           8
        .value_kind:     global_buffer
    .group_segment_fixed_size: 24704
    .kernarg_segment_align: 8
    .kernarg_segment_size: 40
    .language:       OpenCL C
    .language_version:
      - 2
      - 0
    .max_flat_workgroup_size: 1024
    .name:           _Z12giou_partialPK15HIP_vector_typeIfLj4EES2_S2_PKiPS_IfLj2EE
    .private_segment_fixed_size: 0
    .sgpr_count:     34
    .sgpr_spill_count: 0
    .symbol:         _Z12giou_partialPK15HIP_vector_typeIfLj4EES2_S2_PKiPS_IfLj2EE.kd
    .uniform_work_group_size: 1
    .uses_dynamic_stack: false
    .vgpr_count:     26
    .vgpr_spill_count: 0
    .wavefront_size: 64
  - .agpr_count:     0
    .args:
      - .actual_access:  read_only
        .address_space:  global
        .offset:         0
        .size:           8
        .value_kind:     global_buffer
      - .actual_access:  write_only
        .address_space:  global
        .offset:         8
        .size:           8
        .value_kind:     global_buffer
    .group_segment_fixed_size: 0
    .kernarg_segment_align: 8
    .kernarg_segment_size: 16
    .language:       OpenCL C
    .language_version:
      - 2
      - 0
    .max_flat_workgroup_size: 64
    .name:           _Z10giou_finalPK15HIP_vector_typeIfLj2EEPf
    .private_segment_fixed_size: 0
    .sgpr_count:     18
    .sgpr_spill_count: 0
    .symbol:         _Z10giou_finalPK15HIP_vector_typeIfLj2EEPf.kd
    .uniform_work_group_size: 1
    .uses_dynamic_stack: false
    .vgpr_count:     18
    .vgpr_spill_count: 0
    .wavefront_size: 64
